# dilated attention units: tiles resident, no barriers between a wave's three steps (one barrier before the unit's DMA, one after its tiles land)
# speedup vs baseline: 1.0305x; 1.0061x over previous
; #define ATT_WAIT_BAR(N) asm volatile("s_waitcnt vmcnt(" #N ") lgkmcnt(0)\n\ts_barrier" ::: "memory")
; #define ATT_DMA(t, slot) do { glds16(ksrc + (long)(t) * tstep, (unsigned)__builtin_amdgcn_readfirstlane(kdst + (slot))); glds16(vsrc + (long)(t) * tstep, (unsigned)__builtin_amdgcn_readfirstlane(vdst + (slot))); } while (0)
; template <class BIAS>
; __device__ __forceinline__ void attn_tiles(char* shm, const UnitIO& io, int t_begin, int t_end, const BIAS& B, int tid) {
;     ...
;     ATT_DMA(t_begin, 0);
;     asm volatile("" :: "v"(qr[0]), "v"(qr[1]), "v"(qr[2]), "v"(qr[3]));
;     const int nt_ = t_end - t_begin; if (nt_ > 1) ATT_DMA(t_begin + 1, SLOTB); if (nt_ > 2) ATT_DMA(t_begin + 2, 2 * SLOTB);
;     f32x16 o[2]; o[0] = f32x16{}; o[1] = f32x16{}; float l_reg = 0.f;
;     if (nt_ > 2) ATT_WAIT_BAR(4); else if (nt_ > 1) ATT_WAIT_BAR(2); else ATT_WAIT_BAR(0);
; __device__ __forceinline__ void dil_unit(Frame& F, const AttnBufs& A, int b, int h, int g, int r, int c) {
;     char* shm = (char*)F.lds; const int tid = F.tid, lane = tid & 63, r32 = lane & 31, hi = lane >> 5, w = F.wave;
;     const int dil = (g == 0) ? 1 : (g == 1 ? 4 : 16);
;     const int i0 = 256 * c;
;     att::BiasDil B; B.sd = exp2f(-8.0f * (float)(h - 10 + 1) / 10.0f) * LOG2E * (float)dil; B.qrel = 128 + w * 32 + r32; B.hi = hi; B.w = w; B.setup(r32);
;     const long tok_q0 = (long)b * SEQ + r + (long)dil * (i0 + w * 32);
;     const long tok_k0 = (long)b * SEQ + r + (long)dil * (i0 - 128);
;     const long bo = (long)b * (long)BADJ;
;     att::UnitIO io; io.Q = A.Q + bo + tok_q0 * DM + h * 64; io.qstride = (long)DM * dil; io.K0 = A.K + bo + tok_k0 * DM + h * 64; io.V0 = A.V + bo + tok_k0 * DM + h * 64; io.kstride = (long)DM * dil;
;     io.O = A.OD + (size_t)g * OD_BRANCH + tok_q0 * 384 + (h - 10) * 64; io.ostride = (long)384 * dil; io.L = A.LD + (size_t)g * LD_BRANCH + tok_q0 * 8 + (h - 10); io.lstride = (long)8 * dil; io.norm = false;
;     ...
;     att::attn_tiles(shm, io, 5, 6, B, tid);
;     ...
;     att::attn_tiles(shm, io, c == 0 ? 2 : 0, 6, B, tid);
.LBB0_363:
	s_lshl_b32 s56, s74, 5
	v_readlane_b32 s2, v254, 30
	s_or_b32 s56, s56, s2
	s_mul_hi_u32 s57, s56, 0xaaaaaaab
	s_lshr_b32 s75, s57, 5
	s_mul_i32 s57, s75, 48
	s_sub_i32 s66, s56, s57
	s_lshr_b32 s2, s66, 4
	s_and_b32 s67, s66, 15
	s_cmp_lt_u32 s66, 16
	s_cselect_b64 s[62:63], -1, 0
	s_cmp_eq_u32 s2, 1
	s_cselect_b64 s[64:65], -1, 0
	s_bfe_u32 s68, s66, 0x20002
	s_and_b64 s[56:57], s[64:65], exec
	s_cselect_b32 s68, s68, s67
	s_and_b64 s[56:57], s[62:63], exec
	s_cselect_b32 s68, 0, s68
	s_and_b32 s66, s66, 3
	s_and_b64 s[56:57], s[64:65], exec
	s_cselect_b32 s66, s66, 0
	s_and_b64 s[56:57], s[62:63], exec
	s_cselect_b32 s76, s67, s66
	s_and_b64 s[56:57], s[64:65], exec
	s_cselect_b32 s66, 4, 16
	s_and_b64 s[56:57], s[62:63], exec
	s_cselect_b32 s80, 1, s66
	s_not_b32 s56, s75
	s_lshl_b32 s56, s56, 3
	v_cvt_f32_i32_e32 v0, s56
	s_mov_b32 s84, 0x41200000
	s_mov_b32 s85, 0x41300000
	s_lshl_b32 s69, s76, 8
	v_div_scale_f32 v2, s[56:57], s84, s84, v0
	v_rcp_f32_e32 v3, v2
	s_mov_b32 s56, 0xc2fc0000
	v_readlane_b32 s70, v254, 38
	v_readlane_b32 s71, v254, 39
	v_fma_f32 v4, -v2, v3, 1.0
	v_fmac_f32_e32 v3, v4, v3
	v_div_scale_f32 v4, vcc, v0, s84, v0
	v_mul_f32_e32 v5, v4, v3
	v_fma_f32 v6, -v2, v5, v4
	v_fmac_f32_e32 v5, v6, v3
	v_fma_f32 v2, -v2, v5, v4
	v_div_fmas_f32 v2, v2, v3, v5
	v_div_fixup_f32 v0, v2, s84, v0
	v_cmp_gt_f32_e32 vcc, s56, v0
	s_and_b64 s[56:57], vcc, exec
	v_readlane_b32 s56, v254, 48
	s_cselect_b32 s81, 0xffffffc0, 0
	s_add_i32 s56, s69, s56
	s_or_b32 s68, s70, s68
	s_ashr_i32 s57, s56, 31
	s_and_b64 s[66:67], s[64:65], exec
	s_cselect_b32 s70, 2, 4
	s_and_b64 s[66:67], s[62:63], exec
	s_cselect_b32 s70, 0, s70
	s_lshl_b64 s[56:57], s[56:57], s70
	s_add_u32 s66, s56, s68
	s_addc_u32 s67, s57, s71
	s_add_i32 s56, s69, 0xffffff80
	s_ashr_i32 s57, s56, 31
	s_lshl_b64 s[56:57], s[56:57], s70
	s_add_u32 s56, s56, s68
	s_addc_u32 s57, s57, s71
	s_lshl_b64 s[68:69], s[66:67], 11
	v_readlane_b32 s70, v254, 42
	s_add_u32 s68, s70, s68
	v_readlane_b32 s70, v254, 45
	s_addc_u32 s69, s70, s69
	s_lshl_b32 s70, s75, 6
	s_lshl_b32 s77, s75, 7
	v_writelane_b32 v255, s70, 49
	s_add_u32 s70, s68, s77
	s_addc_u32 s71, s69, 0
	s_lshl_b64 s[68:69], s[56:57], 11
	v_readlane_b32 s56, v254, 49
	s_add_u32 s56, s56, s68
	v_readlane_b32 s57, v254, 50
	s_addc_u32 s57, s57, s69
	s_add_u32 s56, s56, s77
	s_addc_u32 s57, s57, 0
	v_readlane_b32 s78, v254, 53
	s_add_u32 s68, s78, s68
	v_readlane_b32 s78, v254, 54
	s_addc_u32 s69, s78, s69
	s_add_u32 s68, s68, s77
	s_addc_u32 s69, s69, 0
	s_cmp_eq_u32 s76, 0
	v_readfirstlane_b32 s77, v232
	s_cselect_b32 s88, 2, 0
	s_ashr_i32 s76, s77, 6
	s_and_b64 s[78:79], s[64:65], exec
	s_cselect_b32 s82, 12, 14
	s_and_b64 s[78:79], s[62:63], exec
	s_cselect_b32 s83, 10, s82
	v_lshlrev_b64 v[2:3], s83, v[146:147]
	v_lshl_add_u64 v[2:3], v[2:3], 1, s[70:71]
	v_mov_b32_e32 v149, v1
	v_lshl_add_u64 v[2:3], v[2:3], 0, v[148:149]
	flat_load_dwordx4 v[98:101], v[2:3] offset:1280
	flat_load_dwordx4 v[102:105], v[2:3] offset:1312
	flat_load_dwordx4 v[106:109], v[2:3] offset:1344
	flat_load_dwordx4 v[110:113], v[2:3] offset:1376
	v_cndmask_b32_e32 v4, 0, v224, vcc
	v_add_f32_e32 v0, v0, v4
	v_exp_f32_e32 v0, v0
	v_cvt_f32_ubyte0_e32 v3, s80
	s_mov_b32 s78, 2.0
	s_mov_b32 s79, 0x40400000
	v_ldexp_f32 v0, v0, s81
	v_mul_f32_e32 v0, 0x3fb8aa3b, v0
	v_mul_f32_e32 v155, v0, v3
	v_mov_b32_e32 v0, v155
	v_pk_mul_f32 v[158:159], v[0:1], s[78:79] op_sel_hi:[0,1]
	s_mov_b32 s78, 0x41000000
	s_mov_b32 s79, 0x41100000
	v_pk_mul_f32 v[160:161], v[0:1], s[78:79] op_sel_hi:[0,1]
	s_mov_b32 s78, 0x41800000
	s_mov_b32 s79, 0x41880000
	v_pk_mul_f32 v[164:165], v[0:1], s[78:79] op_sel_hi:[0,1]
	s_mov_b32 s78, 0x41900000
	s_mov_b32 s79, 0x41980000
	v_pk_mul_f32 v[166:167], v[0:1], s[78:79] op_sel_hi:[0,1]
	s_mov_b32 s78, 0x41c00000
	s_mov_b32 s79, 0x41c80000
	v_pk_mul_f32 v[168:169], v[0:1], s[78:79] op_sel_hi:[0,1]
	s_mov_b32 s78, 0x41d00000
	s_mov_b32 s79, 0x41d80000
	v_pk_mul_f32 v[170:171], v[0:1], s[78:79] op_sel_hi:[0,1]
	s_lshl_b32 s70, s76, 4
	s_ashr_i32 s79, s77, 3
	v_pk_mul_f32 v[162:163], v[0:1], s[84:85] op_sel_hi:[0,1]
	s_lshl_b32 s80, s76, 3
	s_lshl_b32 s78, s76, 10
	v_and_or_b32 v0, s70, 48, v178
	s_and_b32 s82, s79, 0xffffffe0
	v_lshlrev_b64 v[4:5], s83, v[194:195]
	s_ashr_i32 s81, s80, 31
	s_add_i32 s79, s78, 0x8000
	v_lshlrev_b64 v[6:7], s83, v[0:1]
	s_ashr_i32 s83, s82, 31
	v_lshl_add_u64 v[4:5], v[4:5], 1, s[56:57]
	s_and_b64 s[56:57], s[64:65], exec
	v_lshl_add_u64 v[172:173], s[80:81], 1, v[4:5]
	v_lshlrev_b32_e32 v248, 11, v246
	v_mov_b32_e32 v249, s2
	v_lshlrev_b32_e32 v249, 1, v249
	v_lshlrev_b32_e32 v248, v249, v248
	v_add_u32_e32 v248, v248, v247
	v_ashrrev_i32_e32 v249, 31, v248
	v_lshl_add_u64 v[172:173], v[172:173], 0, v[248:249]
	v_lshl_add_u64 v[4:5], v[6:7], 1, s[68:69]
	s_cselect_b32 s68, 18, 20
	s_and_b64 s[56:57], s[62:63], exec
	s_mov_b32 s89, s3
	s_cselect_b32 s80, 16, s68
	v_mov_b32_e32 v151, v1
	v_lshl_add_u64 v[4:5], s[82:83], 1, v[4:5]
	v_lshl_add_u64 v[174:175], v[4:5], 0, v[150:151]
	v_writelane_b32 v254, s2, 9
	v_mov_b32_e32 v2, 0
	s_mov_b32 s81, s88
	s_mov_b32 s100, s88
	s_barrier
.Ldl_pro:
	s_mov_b32 s101, 0
	s_lshl_b64 s[56:57], s[100:101], s80
	s_lshl_b64 s[56:57], s[56:57], 1
	s_add_u32 s56, s56, 0x500
	s_addc_u32 s57, s57, 0
	v_lshl_add_u64 v[4:5], v[172:173], 0, s[56:57]
	v_lshl_add_u64 v[6:7], v[174:175], 0, s[56:57]
	s_lshl_b32 s68, s100, 13
	s_cmp_gt_u32 s100, 3
	s_cselect_b32 s69, 0x14000, 0
	s_add_i32 s68, s68, s69
	s_add_i32 s69, s68, s78
	s_mov_b32 m0, s69
	s_add_i32 s68, s68, s79
	global_load_lds_dwordx4 v[4:5], off
	s_mov_b32 m0, s68
	s_nop 0
	global_load_lds_dwordx4 v[6:7], off
	s_add_i32 s100, s100, 1
	s_cmp_lt_u32 s100, 6
	s_cbranch_scc1 .Ldl_pro
	s_mov_b32 s88, s73
	s_waitcnt vmcnt(0) lgkmcnt(0)
	s_barrier
	v_mov_b32_e32 v16, v2
	v_mov_b32_e32 v17, v2
	v_mul_f32_e32 v156, 0x42000000, v155
	v_mov_b32_e32 v3, v2
	v_mov_b32_e32 v4, v2
	v_mov_b32_e32 v5, v2
	v_mov_b32_e32 v6, v2
	v_mov_b32_e32 v7, v2
	v_mov_b32_e32 v8, v2
	v_mov_b32_e32 v9, v2
	v_mov_b32_e32 v10, v2
	v_mov_b32_e32 v11, v2
	v_mov_b32_e32 v12, v2
	v_mov_b32_e32 v13, v2
	v_mov_b32_e32 v14, v2
	v_mov_b32_e32 v15, v2
	v_mov_b64_e32 v[32:33], v[16:17]
	v_mul_f32_e32 v149, 0x42800000, v155
	v_mul_f32_e32 v154, 0, v155
	v_writelane_b32 v254, s3, 10
	v_mul_f32_e32 v0, v155, v196
	v_mov_b32_e32 v176, v156
	v_mov_b32_e32 v177, v156
	v_mov_b64_e32 v[30:31], v[14:15]
	v_mov_b64_e32 v[28:29], v[12:13]
	v_mov_b64_e32 v[26:27], v[10:11]
	v_mov_b64_e32 v[24:25], v[8:9]
	v_mov_b64_e32 v[22:23], v[6:7]
	v_mov_b64_e32 v[20:21], v[4:5]
	v_mov_b64_e32 v[18:19], v[2:3]
	v_mov_b32_e32 v151, v2
	s_branch .LBB0_365

; #define ATT_WAIT_BAR(N) asm volatile("s_waitcnt vmcnt(" #N ") lgkmcnt(0)\n\ts_barrier" ::: "memory")
; template <class BIAS>
; __device__ __forceinline__ void attn_tiles(char* shm, const UnitIO& io, int t_begin, int t_end, const BIAS& B, int tid) {
;     ...
;         if (rem > 3) ATT_WAIT_BAR(4); else if (rem > 2) ATT_WAIT_BAR(2); else ATT_WAIT_BAR(0);
.Ldl_endstep:
	s_branch .LBB0_364
